# baseline (speedup 1.0000x reference)
.LBB2_48:
	v_readlane_b32 s2, v35, 0
	v_readlane_b32 s3, v35, 16
	s_max_i32 s2, s2, s3
	v_readlane_b32 s3, v35, 32
	v_readlane_b32 s4, v35, 48
	s_nop 0
	v_mov_b32_e32 v2, s3
	v_mov_b32_e32 v3, s4
	v_max3_i32 v2, s2, v2, v3
	s_mov_b32 s2, 3
	v_readfirstlane_b32 s3, v2
	s_add_i32 s3, s3, 3
	s_mul_hi_i32 s3, s3, 0x55555556
	s_lshr_b32 s4, s3, 31
	s_add_i32 s3, s3, s4
	s_mul_i32 s3, s3, 3
	s_setprio 3
	s_cmp_gt_i32 s3, 33
	s_cbranch_scc1 .Ll1g_prc
	s_setprio 2
	s_cmp_gt_i32 s3, 24
	s_cbranch_scc1 .Ll1g_prc
	s_setprio 1

.LBB2_57:
	s_endpgm
	s_nop 0
	s_nop 0
	s_nop 0
	s_nop 0
	s_nop 0
	s_nop 0
	s_nop 0
	s_nop 0
	s_nop 0
	s_nop 0
	s_nop 0
	s_nop 0
	s_nop 0
	s_nop 0
	s_nop 0
	s_nop 0
	s_nop 0
	s_nop 0
	s_nop 0
	s_nop 0
	s_nop 0
	s_nop 0
	s_nop 0
	s_nop 0
	s_nop 0
	s_nop 0
	s_nop 0
	s_nop 0
	s_nop 0
	s_nop 0
	s_nop 0
	s_nop 0
	s_nop 0
	s_nop 0
	s_nop 0
	s_nop 0
	s_nop 0
	s_nop 0
	s_nop 0
	s_nop 0
	s_nop 0
	s_nop 0
	s_nop 0
	s_nop 0
	s_nop 0
	s_nop 0
	s_nop 0
	s_nop 0
	s_nop 0
	s_nop 0
	s_nop 0
	s_nop 0
	s_nop 0
	s_nop 0
	s_nop 0
	s_nop 0
	s_nop 0
	s_endpgm

.LBB3_32:
	s_or_b64 exec, exec, s[6:7]
	v_add_f32_e32 v17, 0, v17
	v_add_f32_e32 v13, v17, v13
	v_add_f32_e32 v9, v13, v9
	v_cvt_f32_i32_e32 v17, v37
	v_max_f32_e32 v22, v11, v11
	v_add_f32_dpp v9, v9, v9 quad_perm:[1,0,3,2] row_mask:0xf bank_mask:0xf
	v_max_f32_e32 v22, 0xff800000, v22
	v_max3_f32 v22, v22, v7, v14
	v_add_f32_dpp v9, v9, v9 quad_perm:[2,3,0,1] row_mask:0xf bank_mask:0xf
	s_nop 1
	v_add_f32_dpp v9, v9, v9 row_half_mirror row_mask:0xf bank_mask:0xf
	v_mov_b32_e32 v13, v9
	s_nop 1
	v_mov_b32_dpp v13, v13 row_mirror row_mask:0xf bank_mask:0xf
	s_waitcnt vmcnt(0)
	v_pk_add_f32 v[8:9], v[8:9], v[12:13]
	v_max_f32_e32 v12, 1.0, v17
	v_div_scale_f32 v13, s[6:7], v12, v12, v9
	v_rcp_f32_e32 v17, v13
	s_movk_i32 s7, 0x180
	s_mov_b32 s6, 0
	v_fma_f32 v23, -v13, v17, 1.0
	v_fmac_f32_e32 v17, v23, v17
	v_div_scale_f32 v23, vcc, v9, v12, v9
	v_mul_f32_e32 v24, v23, v17
	v_fma_f32 v25, -v13, v24, v23
	v_fmac_f32_e32 v24, v25, v17
	v_fma_f32 v13, -v13, v24, v23
	v_div_fmas_f32 v13, v13, v17, v24
	v_div_fixup_f32 v9, v13, v12, v9
	v_add_f32_e32 v8, v8, v9
	v_mul_f32_e32 v9, 0x3e4ccccd, v8
	v_cmp_lt_f32_e32 vcc, 0, v8
	s_nop 1
	v_cndmask_b32_e32 v8, v9, v8, vcc
	v_cmp_eq_u32_e32 vcc, v33, v37
	s_nop 0
	v_max_f32_dpp v9, v22, v22 quad_perm:[1,0,3,2] row_mask:0xf bank_mask:0xf
	s_nop 1
	v_max_f32_dpp v9, v9, v9 quad_perm:[2,3,0,1] row_mask:0xf bank_mask:0xf
	s_nop 1
	v_max_f32_dpp v9, v9, v9 row_half_mirror row_mask:0xf bank_mask:0xf
	s_nop 1
	v_max_f32_dpp v12, v9, v9 row_mirror row_mask:0xf bank_mask:0xf
	v_max_f32_e32 v9, v12, v8
	v_sub_f32_e32 v11, v11, v9
	v_mul_f32_e32 v11, 0x3fb8aa3b, v11
	v_sub_f32_e32 v7, v7, v9
	v_exp_f32_e32 v11, v11
	v_mul_f32_e32 v7, 0x3fb8aa3b, v7
	v_sub_f32_e32 v13, v14, v9
	v_exp_f32_e32 v7, v7
	v_mul_f32_e32 v13, 0x3fb8aa3b, v13
	v_exp_f32_e32 v13, v13
	v_add_f32_e32 v12, 0, v11
	v_cndmask_b32_e64 v12, 0, v12, s[0:1]
	v_cndmask_b32_e64 v14, 0, v7, s[2:3]
	v_add_f32_e32 v12, v12, v14
	v_cndmask_b32_e64 v14, 0, v13, s[4:5]
	v_add_f32_e32 v12, v12, v14
	v_sub_f32_e32 v8, v8, v9
	v_mul_f32_e32 v8, 0x3fb8aa3b, v8
	v_exp_f32_e32 v8, v8
	v_add_f32_dpp v9, v12, v12 quad_perm:[1,0,3,2] row_mask:0xf bank_mask:0xf
	s_nop 1
	v_add_f32_dpp v9, v9, v9 quad_perm:[2,3,0,1] row_mask:0xf bank_mask:0xf
	s_nop 1
	v_add_f32_dpp v9, v9, v9 row_half_mirror row_mask:0xf bank_mask:0xf
	s_nop 1
	v_add_f32_dpp v9, v9, v9 row_mirror row_mask:0xf bank_mask:0xf
	v_add_f32_e32 v9, v8, v9
	v_add_f32_e32 v9, 0x24e69595, v9
	v_rcp_f32_e32 v12, v9
	v_or_b32_e32 v9, s22, v36
	v_mul_lo_u32 v9, v9, s7
	v_or_b32_e32 v17, v9, v38
	v_mul_f32_e32 v22, v8, v12
	v_mul_f32_e32 v8, v12, v11
	v_cndmask_b32_e32 v9, 0, v22, vcc
	v_cmp_eq_u32_e32 vcc, v16, v37
	v_cndmask_b32_e64 v14, v9, v8, s[0:1]
	v_mul_f32_e32 v7, v12, v7
	v_cndmask_b32_e32 v8, 0, v22, vcc
	v_cndmask_b32_e64 v8, v8, v7, s[2:3]
	v_mov_b32_e32 v9, v10
	v_cmp_eq_u32_e32 vcc, v21, v37
	ds_write2_b64 v17, v[14:15], v[8:9] offset1:16
	v_mul_f32_e32 v7, v12, v13
	v_cndmask_b32_e32 v8, 0, v22, vcc
	v_readlane_b32 s0, v37, 0
	v_cndmask_b32_e64 v8, v8, v7, s[4:5]
	v_mov_b32_e32 v9, v6
	s_mul_i32 s7, s22, 0x180
	s_add_i32 s2, s0, 1
	ds_write_b64 v17, v[8:9] offset:256
	s_setprio 3
	v_readlane_b32 s1, v37, 16
	v_readlane_b32 s2, v37, 32
	v_readlane_b32 s3, v37, 48
	v_or_b32_e32 v6, s22, v36
	v_mul_u32_u24_e32 v6, 0x180, v6
	v_mov_b32_e32 v48, 0
	v_mov_b32_e32 v49, 0
	s_max_i32 s0, s0, s1
	s_max_i32 s2, s2, s3
	s_max_i32 s0, s0, s2
	s_add_i32 s0, s0, 4
	s_and_b32 s0, s0, -4
	s_cmp_gt_i32 s0, 32
	s_cbranch_scc1 .Ll2g_prc
	s_setprio 2
	s_cmp_gt_i32 s0, 24
	s_cbranch_scc1 .Ll2g_prc
	s_setprio 1

.LBB3_55:
	s_waitcnt vmcnt(1)
	v_add_f32_e32 v7, v8, v14
	v_add_f32_e32 v7, v13, v7
	v_mul_f32_e32 v14, 0x3e4ccccd, v7
	v_cmp_lt_f32_e32 vcc, 0, v7
	s_nop 1
	v_cndmask_b32_e32 v7, v14, v7, vcc
	s_or_b64 exec, exec, s[6:7]
	v_mov_b32_e32 v14, 0xff800000
	s_and_saveexec_b64 s[6:7], s[4:5]
	s_cbranch_execnz .LBB3_31
	s_branch .LBB3_32
	s_nop 0
	s_nop 0
	s_nop 0
	s_nop 0
	s_nop 0
	s_nop 0
	s_nop 0
	s_nop 0
	s_nop 0
	s_endpgm

.Lpairs_no3a:
	s_waitcnt vmcnt(16)
	ds_write_b128 v72, v[52:55]
	ds_write_b128 v72, v[56:59] offset:8192
	s_waitcnt lgkmcnt(0)
	s_barrier
	s_mov_b32 s36, s32
	s_mov_b32 s37, s33
	s_cmpk_lt_i32 s34, 0x30d4
	s_cbranch_scc0 .Lpairs_joint
	s_setprio 2
	s_waitcnt vmcnt(5)
	ds_read_b128 v[52:55], v2 offset:0
	ds_read_b128 v[56:59], v2 offset:1024
	ds_read_b128 v[60:63], v2 offset:2048
	ds_read_b128 v[64:67], v2 offset:3072
	s_waitcnt lgkmcnt(3)
	v_mfma_f32_16x16x32_f16 v[16:19], v[20:23], v[52:55], 0
	ds_read_b128 v[52:55], v2 offset:4096
	s_waitcnt lgkmcnt(3)
	v_mfma_f32_16x16x32_f16 v[16:19], v[24:27], v[56:59], v[16:19]
	ds_read_b128 v[56:59], v2 offset:5120
	s_waitcnt lgkmcnt(3)
	v_mfma_f32_16x16x32_f16 v[16:19], v[28:31], v[60:63], v[16:19]
	ds_read_b128 v[60:63], v2 offset:6144
	s_waitcnt lgkmcnt(3)
	v_mfma_f32_16x16x32_f16 v[16:19], v[32:35], v[64:67], v[16:19]
	ds_read_b128 v[64:67], v2 offset:7168
	s_nop 7
	v_add_f32_e32 v16, v4, v16
	v_add_f32_e32 v17, v4, v17
	v_add_f32_e32 v18, v4, v18
	v_add_f32_e32 v19, v4, v19
	v_max_f32_e32 v16, 0, v16
	v_max_f32_e32 v17, 0, v17
	v_max_f32_e32 v18, 0, v18
	v_max_f32_e32 v19, 0, v19
	v_mul_f32_e32 v12, v8, v16
	v_mul_f32_e32 v13, v8, v17
	v_mul_f32_e32 v14, v8, v18
	v_mul_f32_e32 v15, v8, v19
	s_waitcnt lgkmcnt(3)
	v_mfma_f32_16x16x32_f16 v[16:19], v[20:23], v[52:55], 0
	ds_read_b128 v[52:55], v2 offset:8192
	s_waitcnt lgkmcnt(3)
	v_mfma_f32_16x16x32_f16 v[16:19], v[24:27], v[56:59], v[16:19]
	ds_read_b128 v[56:59], v2 offset:9216
	s_waitcnt lgkmcnt(3)
	v_mfma_f32_16x16x32_f16 v[16:19], v[28:31], v[60:63], v[16:19]
	ds_read_b128 v[60:63], v2 offset:10240
	s_waitcnt lgkmcnt(3)
	v_mfma_f32_16x16x32_f16 v[16:19], v[32:35], v[64:67], v[16:19]
	ds_read_b128 v[64:67], v2 offset:11264
	s_nop 7
	v_add_f32_e32 v16, v5, v16
	v_add_f32_e32 v17, v5, v17
	v_add_f32_e32 v18, v5, v18
	v_add_f32_e32 v19, v5, v19
	v_max_f32_e32 v16, 0, v16
	v_max_f32_e32 v17, 0, v17
	v_max_f32_e32 v18, 0, v18
	v_max_f32_e32 v19, 0, v19
	v_fmac_f32_e32 v12, v9, v16
	v_fmac_f32_e32 v13, v9, v17
	v_fmac_f32_e32 v14, v9, v18
	v_fmac_f32_e32 v15, v9, v19
	s_waitcnt lgkmcnt(3)
	v_mfma_f32_16x16x32_f16 v[16:19], v[20:23], v[52:55], 0
	ds_read_b128 v[52:55], v2 offset:12288
	s_waitcnt lgkmcnt(3)
	v_mfma_f32_16x16x32_f16 v[16:19], v[24:27], v[56:59], v[16:19]
	ds_read_b128 v[56:59], v2 offset:13312
	s_waitcnt lgkmcnt(3)
	v_mfma_f32_16x16x32_f16 v[16:19], v[28:31], v[60:63], v[16:19]
	ds_read_b128 v[60:63], v2 offset:14336
	s_waitcnt lgkmcnt(3)
	v_mfma_f32_16x16x32_f16 v[16:19], v[32:35], v[64:67], v[16:19]
	ds_read_b128 v[64:67], v2 offset:15360
	s_nop 7
	v_add_f32_e32 v16, v6, v16
	v_add_f32_e32 v17, v6, v17
	v_add_f32_e32 v18, v6, v18
	v_add_f32_e32 v19, v6, v19
	v_max_f32_e32 v16, 0, v16
	v_max_f32_e32 v17, 0, v17
	v_max_f32_e32 v18, 0, v18
	v_max_f32_e32 v19, 0, v19
	v_fmac_f32_e32 v12, v10, v16
	v_fmac_f32_e32 v13, v10, v17
	v_fmac_f32_e32 v14, v10, v18
	v_fmac_f32_e32 v15, v10, v19
	s_waitcnt lgkmcnt(3)
	v_mfma_f32_16x16x32_f16 v[16:19], v[20:23], v[52:55], 0
	s_waitcnt lgkmcnt(2)
	v_mfma_f32_16x16x32_f16 v[16:19], v[24:27], v[56:59], v[16:19]
	s_waitcnt lgkmcnt(1)
	v_mfma_f32_16x16x32_f16 v[16:19], v[28:31], v[60:63], v[16:19]
	s_waitcnt lgkmcnt(0)
	v_mfma_f32_16x16x32_f16 v[16:19], v[32:35], v[64:67], v[16:19]
	s_nop 7
	v_add_f32_e32 v16, v7, v16
	v_add_f32_e32 v17, v7, v17
	v_add_f32_e32 v18, v7, v18
	v_add_f32_e32 v19, v7, v19
	v_max_f32_e32 v16, 0, v16
	v_max_f32_e32 v17, 0, v17
	v_max_f32_e32 v18, 0, v18
	v_max_f32_e32 v19, 0, v19
	v_fmac_f32_e32 v12, v11, v16
	v_fmac_f32_e32 v13, v11, v17
	v_fmac_f32_e32 v14, v11, v18
	v_fmac_f32_e32 v15, v11, v19
	v_add_f32_dpp v12, v12, v12 quad_perm:[1,0,3,2] row_mask:0xf bank_mask:0xf
	v_add_f32_dpp v13, v13, v13 quad_perm:[1,0,3,2] row_mask:0xf bank_mask:0xf
	v_add_f32_dpp v14, v14, v14 quad_perm:[1,0,3,2] row_mask:0xf bank_mask:0xf
	v_add_f32_dpp v15, v15, v15 quad_perm:[1,0,3,2] row_mask:0xf bank_mask:0xf
	v_add_f32_dpp v12, v12, v12 quad_perm:[2,3,0,1] row_mask:0xf bank_mask:0xf
	v_add_f32_dpp v13, v13, v13 quad_perm:[2,3,0,1] row_mask:0xf bank_mask:0xf
	v_add_f32_dpp v14, v14, v14 quad_perm:[2,3,0,1] row_mask:0xf bank_mask:0xf
	v_add_f32_dpp v15, v15, v15 quad_perm:[2,3,0,1] row_mask:0xf bank_mask:0xf
	v_add_f32_dpp v12, v12, v12 row_half_mirror row_mask:0xf bank_mask:0xf
	v_add_f32_dpp v13, v13, v13 row_half_mirror row_mask:0xf bank_mask:0xf
	v_add_f32_dpp v14, v14, v14 row_half_mirror row_mask:0xf bank_mask:0xf
	v_add_f32_dpp v15, v15, v15 row_half_mirror row_mask:0xf bank_mask:0xf
	v_add_f32_dpp v12, v12, v12 row_mirror row_mask:0xf bank_mask:0xf
	v_add_f32_dpp v13, v13, v13 row_mirror row_mask:0xf bank_mask:0xf
	v_add_f32_dpp v14, v14, v14 row_mirror row_mask:0xf bank_mask:0xf
	v_add_f32_dpp v15, v15, v15 row_mirror row_mask:0xf bank_mask:0xf
	s_lshl_b32 s3, s36, 6
	s_add_u32 s24, s16, s3
	s_addc_u32 s25, s17, 0
	v_cndmask_b32_e64 v12, v12, v13, s[20:21]
	s_nop 0
	v_cndmask_b32_e64 v12, v12, v14, s[22:23]
	s_nop 0
	v_cndmask_b32_e64 v12, v12, v15, s[26:27]
	s_nop 0
	v_add_f32_e32 v12, s18, v12
	s_mov_b64 s[30:31], exec
	s_mov_b64 exec, s[28:29]
	global_store_dword v0, v12, s[24:25]
	s_mov_b64 exec, s[30:31]
	s_waitcnt vmcnt(0)
	v_lshl_or_b32 v70, v68, 7, v76
	v_lshl_or_b32 v71, v69, 7, v76
	global_load_dwordx4 v[20:23], v70, s[4:5]
	global_load_dwordx4 v[24:27], v70, s[4:5] offset:64
	global_load_dwordx4 v[28:31], v71, s[4:5]
	global_load_dwordx4 v[32:35], v71, s[4:5] offset:64
	s_mov_b32 s36, s34
